# instruction selection in the DSA indexer: hand-written per-tile body (packed weighted sum on (i,i+1) pairs, key via shift+bitop3, one address computation per tile)
# speedup vs baseline: 1.0026x; 1.0026x over previous
.LBB0_552:
	s_waitcnt vmcnt(0)
	v_mfma_f32_16x16x32_bf16 v[100:103], v[62:65], v[28:31], 0
	v_mfma_f32_16x16x32_bf16 v[104:107], v[62:65], v[20:23], 0
	v_mfma_f32_16x16x32_bf16 v[108:111], v[62:65], v[12:15], 0
	v_mfma_f32_16x16x32_bf16 v[112:115], v[62:65], v[4:7], 0
	v_mfma_f32_16x16x32_bf16 v[100:103], v[58:61], v[24:27], v[100:103]
	v_mfma_f32_16x16x32_bf16 v[104:107], v[58:61], v[16:19], v[104:107]
	v_mfma_f32_16x16x32_bf16 v[108:111], v[58:61], v[8:11], v[108:111]
	v_mfma_f32_16x16x32_bf16 v[112:115], v[58:61], v[0:3], v[112:115]
	v_mul_hi_u32 v129, s25, v76
	v_mad_i32_i24 v130, v129, s24, v76
	v_mov_b32_e32 v140, v67
	v_mov_b32_e32 v142, v69
	v_lshl_add_u32 v128, v130, 5, v129
	v_add_u32_e32 v131, v128, v74
	v_add_u32_e32 v128, 2, v130
	v_cmp_eq_u32_e32 vcc, s21, v128
	v_add3_u32 v133, v129, v74, 1
	v_add_u32_e32 v132, 64, v131
	v_and_b32_e32 v134, 0x7ff, v131
	v_cndmask_b32_e32 v132, v132, v133, vcc
	v_add_u32_e32 v128, 32, v131
	v_lshl_add_u32 v134, v134, 2, v75
	v_and_b32_e32 v135, 0x7ff, v128
	v_add_u32_e32 v128, 32, v132
	v_lshl_add_u32 v135, v135, 2, v75
	v_and_b32_e32 v136, 0x7ff, v132
	v_and_b32_e32 v137, 0x7ff, v128
	v_lshl_add_u32 v136, v136, 2, v75
	v_lshl_add_u32 v137, v137, 2, v75
	v_max_f32_e32 v100, 0, v100
	v_max_f32_e32 v101, 0, v101
	v_max_f32_e32 v102, 0, v102
	v_max_f32_e32 v103, 0, v103
	v_max_f32_e32 v104, 0, v104
	v_max_f32_e32 v105, 0, v105
	v_max_f32_e32 v106, 0, v106
	v_max_f32_e32 v107, 0, v107
	v_max_f32_e32 v108, 0, v108
	v_max_f32_e32 v109, 0, v109
	v_max_f32_e32 v110, 0, v110
	v_max_f32_e32 v111, 0, v111
	v_max_f32_e32 v112, 0, v112
	v_max_f32_e32 v113, 0, v113
	v_max_f32_e32 v114, 0, v114
	v_max_f32_e32 v115, 0, v115
	v_pk_mul_f32 v[120:121], v[100:101], v[66:67] op_sel_hi:[1,0]
	v_pk_add_f32 v[120:121], v[120:121], 0 op_sel_hi:[1,0]
	v_pk_mul_f32 v[116:117], v[104:105], v[140:141] op_sel_hi:[1,0]
	v_pk_add_f32 v[120:121], v[120:121], v[116:117]
	v_pk_mul_f32 v[116:117], v[108:109], v[68:69] op_sel_hi:[1,0]
	v_pk_add_f32 v[120:121], v[120:121], v[116:117]
	v_pk_mul_f32 v[116:117], v[112:113], v[142:143] op_sel_hi:[1,0]
	v_pk_add_f32 v[120:121], v[120:121], v[116:117]
	v_pk_mul_f32 v[122:123], v[102:103], v[66:67] op_sel_hi:[1,0]
	v_pk_add_f32 v[122:123], v[122:123], 0 op_sel_hi:[1,0]
	v_pk_mul_f32 v[118:119], v[106:107], v[140:141] op_sel_hi:[1,0]
	v_pk_add_f32 v[122:123], v[122:123], v[118:119]
	v_pk_mul_f32 v[118:119], v[110:111], v[68:69] op_sel_hi:[1,0]
	v_pk_add_f32 v[122:123], v[122:123], v[118:119]
	v_pk_mul_f32 v[118:119], v[114:115], v[142:143] op_sel_hi:[1,0]
	v_pk_add_f32 v[122:123], v[122:123], v[118:119]
	v_ashrrev_i32_e32 v128, 31, v120
	v_bitop3_b32 v124, v120, v128, s30 bitop3:0x1e
	ds_write_b32 v134, v124
	v_ashrrev_i32_e32 v128, 31, v121
	v_bitop3_b32 v125, v121, v128, s30 bitop3:0x1e
	ds_write_b32 v135, v125
	v_ashrrev_i32_e32 v128, 31, v122
	v_bitop3_b32 v126, v122, v128, s30 bitop3:0x1e
	ds_write_b32 v136, v126
	v_ashrrev_i32_e32 v128, 31, v123
	v_bitop3_b32 v127, v123, v128, s30 bitop3:0x1e
	ds_write_b32 v137, v127
	s_andn2_b64 vcc, exec, s[38:39]
	s_cbranch_vccnz .LBB0_545
	v_mfma_f32_16x16x32_bf16 v[100:103], v[44:47], v[28:31], 0
	v_mfma_f32_16x16x32_bf16 v[104:107], v[44:47], v[20:23], 0
	v_mfma_f32_16x16x32_bf16 v[108:111], v[44:47], v[12:15], 0
	v_mfma_f32_16x16x32_bf16 v[112:115], v[44:47], v[4:7], 0
	v_mfma_f32_16x16x32_bf16 v[100:103], v[54:57], v[24:27], v[100:103]
	v_mfma_f32_16x16x32_bf16 v[104:107], v[54:57], v[16:19], v[104:107]
	v_mfma_f32_16x16x32_bf16 v[108:111], v[54:57], v[8:11], v[108:111]
	v_mfma_f32_16x16x32_bf16 v[112:115], v[54:57], v[0:3], v[112:115]
	v_mul_hi_u32 v129, s25, v79
	v_mad_i32_i24 v130, v129, s24, v79
	v_mov_b32_e32 v140, v67
	v_mov_b32_e32 v142, v69
	v_lshl_add_u32 v128, v130, 5, v129
	v_add_u32_e32 v131, v128, v74
	v_add_u32_e32 v128, 2, v130
	v_cmp_eq_u32_e32 vcc, s21, v128
	v_add3_u32 v133, v129, v74, 1
	v_add_u32_e32 v132, 64, v131
	v_and_b32_e32 v134, 0x7ff, v131
	v_cndmask_b32_e32 v132, v132, v133, vcc
	v_add_u32_e32 v128, 32, v131
	v_lshl_add_u32 v134, v134, 2, v75
	v_and_b32_e32 v135, 0x7ff, v128
	v_add_u32_e32 v128, 32, v132
	v_lshl_add_u32 v135, v135, 2, v75
	v_and_b32_e32 v136, 0x7ff, v132
	v_and_b32_e32 v137, 0x7ff, v128
	v_lshl_add_u32 v136, v136, 2, v75
	v_lshl_add_u32 v137, v137, 2, v75
	v_max_f32_e32 v100, 0, v100
	v_max_f32_e32 v101, 0, v101
	v_max_f32_e32 v102, 0, v102
	v_max_f32_e32 v103, 0, v103
	v_max_f32_e32 v104, 0, v104
	v_max_f32_e32 v105, 0, v105
	v_max_f32_e32 v106, 0, v106
	v_max_f32_e32 v107, 0, v107
	v_max_f32_e32 v108, 0, v108
	v_max_f32_e32 v109, 0, v109
	v_max_f32_e32 v110, 0, v110
	v_max_f32_e32 v111, 0, v111
	v_max_f32_e32 v112, 0, v112
	v_max_f32_e32 v113, 0, v113
	v_max_f32_e32 v114, 0, v114
	v_max_f32_e32 v115, 0, v115
	v_pk_mul_f32 v[120:121], v[100:101], v[66:67] op_sel_hi:[1,0]
	v_pk_add_f32 v[120:121], v[120:121], 0 op_sel_hi:[1,0]
	v_pk_mul_f32 v[116:117], v[104:105], v[140:141] op_sel_hi:[1,0]
	v_pk_add_f32 v[120:121], v[120:121], v[116:117]
	v_pk_mul_f32 v[116:117], v[108:109], v[68:69] op_sel_hi:[1,0]
	v_pk_add_f32 v[120:121], v[120:121], v[116:117]
	v_pk_mul_f32 v[116:117], v[112:113], v[142:143] op_sel_hi:[1,0]
	v_pk_add_f32 v[120:121], v[120:121], v[116:117]
	v_pk_mul_f32 v[122:123], v[102:103], v[66:67] op_sel_hi:[1,0]
	v_pk_add_f32 v[122:123], v[122:123], 0 op_sel_hi:[1,0]
	v_pk_mul_f32 v[118:119], v[106:107], v[140:141] op_sel_hi:[1,0]
	v_pk_add_f32 v[122:123], v[122:123], v[118:119]
	v_pk_mul_f32 v[118:119], v[110:111], v[68:69] op_sel_hi:[1,0]
	v_pk_add_f32 v[122:123], v[122:123], v[118:119]
	v_pk_mul_f32 v[118:119], v[114:115], v[142:143] op_sel_hi:[1,0]
	v_pk_add_f32 v[122:123], v[122:123], v[118:119]
	v_ashrrev_i32_e32 v128, 31, v120
	v_bitop3_b32 v124, v120, v128, s30 bitop3:0x1e
	ds_write_b32 v134, v124
	v_ashrrev_i32_e32 v128, 31, v121
	v_bitop3_b32 v125, v121, v128, s30 bitop3:0x1e
	ds_write_b32 v135, v125
	v_ashrrev_i32_e32 v128, 31, v122
	v_bitop3_b32 v126, v122, v128, s30 bitop3:0x1e
	ds_write_b32 v136, v126
	v_ashrrev_i32_e32 v128, 31, v123
	v_bitop3_b32 v127, v123, v128, s30 bitop3:0x1e
	ds_write_b32 v137, v127
	s_andn2_b64 vcc, exec, s[8:9]
	s_cbranch_vccnz .LBB0_545
	v_mfma_f32_16x16x32_bf16 v[100:103], v[40:43], v[28:31], 0
	v_mfma_f32_16x16x32_bf16 v[104:107], v[40:43], v[20:23], 0
	v_mfma_f32_16x16x32_bf16 v[108:111], v[40:43], v[12:15], 0
	v_mfma_f32_16x16x32_bf16 v[112:115], v[40:43], v[4:7], 0
	v_mfma_f32_16x16x32_bf16 v[100:103], v[50:53], v[24:27], v[100:103]
	v_mfma_f32_16x16x32_bf16 v[104:107], v[50:53], v[16:19], v[104:107]
	v_mfma_f32_16x16x32_bf16 v[108:111], v[50:53], v[8:11], v[108:111]
	v_mfma_f32_16x16x32_bf16 v[112:115], v[50:53], v[0:3], v[112:115]
	v_mul_hi_u32 v129, s25, v78
	v_mad_i32_i24 v130, v129, s24, v78
	v_mov_b32_e32 v140, v67
	v_mov_b32_e32 v142, v69
	v_lshl_add_u32 v128, v130, 5, v129
	v_add_u32_e32 v131, v128, v74
	v_add_u32_e32 v128, 2, v130
	v_cmp_eq_u32_e32 vcc, s21, v128
	v_add3_u32 v133, v129, v74, 1
	v_add_u32_e32 v132, 64, v131
	v_and_b32_e32 v134, 0x7ff, v131
	v_cndmask_b32_e32 v132, v132, v133, vcc
	v_add_u32_e32 v128, 32, v131
	v_lshl_add_u32 v134, v134, 2, v75
	v_and_b32_e32 v135, 0x7ff, v128
	v_add_u32_e32 v128, 32, v132
	v_lshl_add_u32 v135, v135, 2, v75
	v_and_b32_e32 v136, 0x7ff, v132
	v_and_b32_e32 v137, 0x7ff, v128
	v_lshl_add_u32 v136, v136, 2, v75
	v_lshl_add_u32 v137, v137, 2, v75
	v_max_f32_e32 v100, 0, v100
	v_max_f32_e32 v101, 0, v101
	v_max_f32_e32 v102, 0, v102
	v_max_f32_e32 v103, 0, v103
	v_max_f32_e32 v104, 0, v104
	v_max_f32_e32 v105, 0, v105
	v_max_f32_e32 v106, 0, v106
	v_max_f32_e32 v107, 0, v107
	v_max_f32_e32 v108, 0, v108
	v_max_f32_e32 v109, 0, v109
	v_max_f32_e32 v110, 0, v110
	v_max_f32_e32 v111, 0, v111
	v_max_f32_e32 v112, 0, v112
	v_max_f32_e32 v113, 0, v113
	v_max_f32_e32 v114, 0, v114
	v_max_f32_e32 v115, 0, v115
	v_pk_mul_f32 v[120:121], v[100:101], v[66:67] op_sel_hi:[1,0]
	v_pk_add_f32 v[120:121], v[120:121], 0 op_sel_hi:[1,0]
	v_pk_mul_f32 v[116:117], v[104:105], v[140:141] op_sel_hi:[1,0]
	v_pk_add_f32 v[120:121], v[120:121], v[116:117]
	v_pk_mul_f32 v[116:117], v[108:109], v[68:69] op_sel_hi:[1,0]
	v_pk_add_f32 v[120:121], v[120:121], v[116:117]
	v_pk_mul_f32 v[116:117], v[112:113], v[142:143] op_sel_hi:[1,0]
	v_pk_add_f32 v[120:121], v[120:121], v[116:117]
	v_pk_mul_f32 v[122:123], v[102:103], v[66:67] op_sel_hi:[1,0]
	v_pk_add_f32 v[122:123], v[122:123], 0 op_sel_hi:[1,0]
	v_pk_mul_f32 v[118:119], v[106:107], v[140:141] op_sel_hi:[1,0]
	v_pk_add_f32 v[122:123], v[122:123], v[118:119]
	v_pk_mul_f32 v[118:119], v[110:111], v[68:69] op_sel_hi:[1,0]
	v_pk_add_f32 v[122:123], v[122:123], v[118:119]
	v_pk_mul_f32 v[118:119], v[114:115], v[142:143] op_sel_hi:[1,0]
	v_pk_add_f32 v[122:123], v[122:123], v[118:119]
	v_ashrrev_i32_e32 v128, 31, v120
	v_bitop3_b32 v124, v120, v128, s30 bitop3:0x1e
	ds_write_b32 v134, v124
	v_ashrrev_i32_e32 v128, 31, v121
	v_bitop3_b32 v125, v121, v128, s30 bitop3:0x1e
	ds_write_b32 v135, v125
	v_ashrrev_i32_e32 v128, 31, v122
	v_bitop3_b32 v126, v122, v128, s30 bitop3:0x1e
	ds_write_b32 v136, v126
	v_ashrrev_i32_e32 v128, 31, v123
	v_bitop3_b32 v127, v123, v128, s30 bitop3:0x1e
	ds_write_b32 v137, v127
	s_andn2_b64 vcc, exec, s[6:7]
	s_cbranch_vccnz .LBB0_545
	v_mfma_f32_16x16x32_bf16 v[100:103], v[32:35], v[28:31], 0
	v_mfma_f32_16x16x32_bf16 v[104:107], v[32:35], v[20:23], 0
	v_mfma_f32_16x16x32_bf16 v[108:111], v[32:35], v[12:15], 0
	v_mfma_f32_16x16x32_bf16 v[112:115], v[32:35], v[4:7], 0
	v_mfma_f32_16x16x32_bf16 v[100:103], v[36:39], v[24:27], v[100:103]
	v_mfma_f32_16x16x32_bf16 v[104:107], v[36:39], v[16:19], v[104:107]
	v_mfma_f32_16x16x32_bf16 v[108:111], v[36:39], v[8:11], v[108:111]
	v_mfma_f32_16x16x32_bf16 v[112:115], v[36:39], v[0:3], v[112:115]
	v_mul_hi_u32 v129, s25, v77
	v_mad_i32_i24 v130, v129, s24, v77
	v_mov_b32_e32 v140, v67
	v_mov_b32_e32 v142, v69
	v_lshl_add_u32 v128, v130, 5, v129
	v_add_u32_e32 v131, v128, v74
	v_add_u32_e32 v128, 2, v130
	v_cmp_eq_u32_e32 vcc, s21, v128
	v_add3_u32 v133, v129, v74, 1
	v_add_u32_e32 v132, 64, v131
	v_and_b32_e32 v134, 0x7ff, v131
	v_cndmask_b32_e32 v132, v132, v133, vcc
	v_add_u32_e32 v128, 32, v131
	v_lshl_add_u32 v134, v134, 2, v75
	v_and_b32_e32 v135, 0x7ff, v128
	v_add_u32_e32 v128, 32, v132
	v_lshl_add_u32 v135, v135, 2, v75
	v_and_b32_e32 v136, 0x7ff, v132
	v_and_b32_e32 v137, 0x7ff, v128
	v_lshl_add_u32 v136, v136, 2, v75
	v_lshl_add_u32 v137, v137, 2, v75
	v_max_f32_e32 v100, 0, v100
	v_max_f32_e32 v101, 0, v101
	v_max_f32_e32 v102, 0, v102
	v_max_f32_e32 v103, 0, v103
	v_max_f32_e32 v104, 0, v104
	v_max_f32_e32 v105, 0, v105
	v_max_f32_e32 v106, 0, v106
	v_max_f32_e32 v107, 0, v107
	v_max_f32_e32 v108, 0, v108
	v_max_f32_e32 v109, 0, v109
	v_max_f32_e32 v110, 0, v110
	v_max_f32_e32 v111, 0, v111
	v_max_f32_e32 v112, 0, v112
	v_max_f32_e32 v113, 0, v113
	v_max_f32_e32 v114, 0, v114
	v_max_f32_e32 v115, 0, v115
	v_pk_mul_f32 v[120:121], v[100:101], v[66:67] op_sel_hi:[1,0]
	v_pk_add_f32 v[120:121], v[120:121], 0 op_sel_hi:[1,0]
	v_pk_mul_f32 v[116:117], v[104:105], v[140:141] op_sel_hi:[1,0]
	v_pk_add_f32 v[120:121], v[120:121], v[116:117]
	v_pk_mul_f32 v[116:117], v[108:109], v[68:69] op_sel_hi:[1,0]
	v_pk_add_f32 v[120:121], v[120:121], v[116:117]
	v_pk_mul_f32 v[116:117], v[112:113], v[142:143] op_sel_hi:[1,0]
	v_pk_add_f32 v[120:121], v[120:121], v[116:117]
	v_pk_mul_f32 v[122:123], v[102:103], v[66:67] op_sel_hi:[1,0]
	v_pk_add_f32 v[122:123], v[122:123], 0 op_sel_hi:[1,0]
	v_pk_mul_f32 v[118:119], v[106:107], v[140:141] op_sel_hi:[1,0]
	v_pk_add_f32 v[122:123], v[122:123], v[118:119]
	v_pk_mul_f32 v[118:119], v[110:111], v[68:69] op_sel_hi:[1,0]
	v_pk_add_f32 v[122:123], v[122:123], v[118:119]
	v_pk_mul_f32 v[118:119], v[114:115], v[142:143] op_sel_hi:[1,0]
	v_pk_add_f32 v[122:123], v[122:123], v[118:119]
	v_ashrrev_i32_e32 v128, 31, v120
	v_bitop3_b32 v124, v120, v128, s30 bitop3:0x1e
	ds_write_b32 v134, v124
	v_ashrrev_i32_e32 v128, 31, v121
	v_bitop3_b32 v125, v121, v128, s30 bitop3:0x1e
	ds_write_b32 v135, v125
	v_ashrrev_i32_e32 v128, 31, v122
	v_bitop3_b32 v126, v122, v128, s30 bitop3:0x1e
	ds_write_b32 v136, v126
	v_ashrrev_i32_e32 v128, 31, v123
	v_bitop3_b32 v127, v123, v128, s30 bitop3:0x1e
	ds_write_b32 v137, v127
	s_branch .LBB0_545
